# in-projection GEMM: weight (B) operand register pipeline two K-tiles deep (second 16-VGPR staging set, steady K-loop unrolled x2, counted waits re-derived)
# baseline (speedup 1.0000x reference)
.LBB0_429:
	s_ashr_i32 s1, s0, 5
	s_lshr_b32 s2, s1, 30
	s_add_i32 s4, s1, s2
	s_and_b32 s2, s4, 0x3ffffc
	s_sub_i32 s1, s1, s2
	s_lshl_b32 s47, s1, 10
	s_lshl_b32 s1, s0, 5
	s_and_b32 s1, s1, 0x300
	s_or_b32 s28, s47, s1
	s_ashr_i32 s29, s28, 31
	s_lshl_b64 s[2:3], s[28:29], 1
	s_add_u32 s6, s36, s2
	s_addc_u32 s7, s37, s3
	s_lshl_b32 s1, s4, 9
	s_lshl_b32 s0, s0, 8
	s_and_b32 s8, s1, 0xfffff800
	s_and_b32 s9, s0, 0x700
	s_or_b32 s50, s8, s9
	v_readfirstlane_b32 s0, v0
	s_lshr_b32 s29, s0, 6
	v_or_b32_e32 v2, s50, v149
	v_lshlrev_b32_e32 v2, 12, v2
	s_lshl_b32 s14, s29, 1
	v_or_b32_e32 v18, v2, v154
	v_add_u32_e32 v19, v2, v163
	v_add_u32_e32 v20, v2, v164
	v_or_b32_e32 v2, s14, v156
	s_and_b32 s1, s29, 4
	s_bfe_u32 s51, s0, 0x20006
	v_and_or_b32 v4, v2, 3, s1
	s_lshr_b32 s1, s0, 1
	s_and_b32 s52, s1, 0x7fffff80
	s_lshl_b32 s1, s51, 7
	s_or_b32 s2, s1, 32
	v_bitop3_b32 v152, s2, v165, v161 bitop3:0xde
	s_or_b32 s2, s1, 64
	v_bitop3_b32 v153, s1, v165, v161 bitop3:0xde
	v_bitop3_b32 v151, s2, v165, v161 bitop3:0xde
	s_or_b32 s1, s1, 0x60
	s_lshl_b32 s2, s29, 10
	v_bitop3_b32 v146, s1, v165, v161 bitop3:0xde
	s_add_i32 s2, s2, 0
	s_mov_b32 s1, m0
	s_mov_b32 m0, s2
	s_nop 0
	global_load_lds_dwordx4 v18, s[16:17]
	s_mov_b32 m0, s1
	s_add_i32 s1, s2, 0x2000
	s_mov_b32 s3, m0
	s_mov_b32 m0, s1
	s_nop 0
	global_load_lds_dwordx4 v19, s[16:17]
	s_mov_b32 m0, s3
	s_add_i32 s1, s2, 0x4000
	v_or_b32_e32 v3, 0x80000, v18
	s_mov_b32 s3, m0
	s_mov_b32 m0, s1
	s_nop 0
	global_load_lds_dwordx4 v3, s[16:17]
	s_mov_b32 m0, s3
	s_add_i32 s1, s2, 0x6000
	s_lshl_b64 s[4:5], s[14:15], 13
	s_add_u32 s4, s6, s4
	v_lshlrev_b32_e32 v4, 5, v4
	v_or_b32_e32 v5, s52, v1
	v_lshlrev_b32_e32 v2, 9, v2
	s_addc_u32 s5, s7, s5
	v_lshlrev_b32_e32 v34, 7, v5
	v_bitop3_b32 v168, v4, v2, v157 bitop3:0xde
	s_mov_b32 s3, m0
	s_mov_b32 m0, s1
	s_nop 0
	global_load_lds_dwordx4 v20, s[16:17]
	s_mov_b32 m0, s3
	global_load_dwordx4 v[216:219], v162, s[4:5]
	s_add_i32 s4, s14, 16
	s_mov_b32 s5, s15
	s_lshl_b64 s[4:5], s[4:5], 13
	s_add_u32 s4, s6, s4
	s_addc_u32 s5, s7, s5
	global_load_dwordx4 v[220:223], v162, s[4:5]
	s_add_i32 s4, s14, 32
	s_mov_b32 s5, s15
	s_lshl_b64 s[4:5], s[4:5], 13
	s_add_u32 s4, s6, s4
	s_addc_u32 s5, s7, s5
	global_load_dwordx4 v[224:227], v162, s[4:5]
	s_add_i32 s4, s14, 48
	s_mov_b32 s5, s15
	s_lshl_b64 s[4:5], s[4:5], 13
	s_add_u32 s4, s6, s4
	s_addc_u32 s5, s7, s5
	s_add_i32 s1, s2, 0x8000
	global_load_dwordx4 v[228:231], v162, s[4:5]
	s_add_i32 s4, s14, 64
	s_mov_b32 s5, s15
	s_lshl_b64 s[4:5], s[4:5], 13
	s_add_u32 s4, s6, s4
	s_addc_u32 s5, s7, s5
	global_load_dwordx4 v[14:17], v162, s[4:5]
	s_add_i32 s4, s14, 80
	s_mov_b32 s5, s15
	s_lshl_b64 s[4:5], s[4:5], 13
	s_add_u32 s4, s6, s4
	s_addc_u32 s5, s7, s5
	global_load_dwordx4 v[10:13], v162, s[4:5]
	s_add_i32 s4, s14, 96
	s_mov_b32 s5, s15
	s_lshl_b64 s[4:5], s[4:5], 13
	s_add_u32 s4, s6, s4
	s_addc_u32 s5, s7, s5
	global_load_dwordx4 v[6:9], v162, s[4:5]
	s_add_i32 s4, s14, 112
	s_mov_b32 s5, s15
	s_lshl_b64 s[4:5], s[4:5], 13
	s_add_u32 s4, s6, s4
	s_addc_u32 s5, s7, s5
	global_load_dwordx4 v[2:5], v162, s[4:5]
	v_or_b32_e32 v21, 0x80, v18
	s_mov_b32 s3, m0
	s_mov_b32 m0, s1
	s_nop 0
	global_load_lds_dwordx4 v21, s[16:17]
	s_mov_b32 m0, s3
	s_add_i32 s1, s2, 0xa000
	v_or_b32_e32 v18, 0x80080, v18
	v_or_b32_e32 v19, 0x80, v19
	s_mov_b32 s3, m0
	s_mov_b32 m0, s1
	s_nop 0
	global_load_lds_dwordx4 v19, s[16:17]
	s_mov_b32 m0, s3
	s_add_i32 s1, s2, 0xc000
	s_mov_b32 s3, m0
	s_mov_b32 m0, s1
	s_nop 0
	global_load_lds_dwordx4 v18, s[16:17]
	s_mov_b32 m0, s3
	v_or_b32_e32 v18, 0x80, v20
	s_add_i32 s4, s14, 0x80
	s_mov_b32 s5, s15
	s_add_i32 s1, s2, 0xe000
	s_mov_b32 s3, m0
	s_mov_b32 m0, s1
	s_nop 0
	global_load_lds_dwordx4 v18, s[16:17]
	s_mov_b32 m0, s3
	s_waitcnt vmcnt(8)
	s_lshl_b64 s[4:5], s[4:5], 13
	v_add_u32_e32 v18, 0, v168
	s_add_u32 s4, s6, s4
	v_add_u32_e32 v172, 0x18000, v18
	s_addc_u32 s5, s7, s5
	ds_write_b128 v172, v[216:219]
	ds_write_b128 v172, v[220:223] offset:8192
	ds_write_b128 v172, v[224:227] offset:16384
	ds_write_b128 v172, v[228:231] offset:24576
	global_load_dwordx4 v[228:231], v162, s[4:5]
	s_add_i32 s4, s14, 0x90
	s_mov_b32 s5, s15
	s_lshl_b64 s[4:5], s[4:5], 13
	s_add_u32 s4, s6, s4
	s_addc_u32 s5, s7, s5
	global_load_dwordx4 v[224:227], v162, s[4:5]
	s_add_i32 s4, s14, 0xa0
	s_mov_b32 s5, s15
	s_lshl_b64 s[4:5], s[4:5], 13
	s_add_u32 s4, s6, s4
	s_addc_u32 s5, s7, s5
	s_addk_i32 s14, 0xb0
	global_load_dwordx4 v[220:223], v162, s[4:5]
	s_lshl_b64 s[4:5], s[14:15], 13
	s_add_u32 s4, s6, s4
	s_addc_u32 s5, s7, s5
	s_lshl_b64 s[0:1], s[0:1], 8
	global_load_dwordx4 v[216:219], v162, s[4:5]
	s_waitcnt lgkmcnt(0)
	s_barrier
	s_and_b32 s1, s1, 0xff
	s_and_b32 s0, s0, 0xffffc000
	v_or_b32_e32 v18, s8, v149
	s_add_u32 s3, s6, s0
	v_or_b32_e32 v18, s9, v18
	v_or_b32_e32 v169, v34, v159
	v_or_b32_e32 v171, v34, v160
	s_addc_u32 s4, s7, s1
	v_lshl_add_u32 v173, v18, 12, v166
	s_mov_b32 s5, 0
	s_mov_b64 s[0:1], 0
	s_mov_b32 s6, 0x8000
	s_mov_b32 s7, 0x10000
	v_mov_b32_e32 v18, 0
	v_mov_b32_e32 v19, v147
	v_mov_b32_e32 v20, v147
	v_mov_b32_e32 v21, v147
	v_mov_b32_e32 v22, 0
	v_mov_b32_e32 v23, v147
	v_mov_b32_e32 v24, v147
	v_mov_b32_e32 v25, v147
	v_mov_b32_e32 v26, 0
	v_mov_b32_e32 v27, v147
	v_mov_b32_e32 v28, v147
	v_mov_b32_e32 v29, v147
	v_mov_b32_e32 v30, 0
	v_mov_b32_e32 v31, v147
	v_mov_b32_e32 v32, v147
	v_mov_b32_e32 v33, v147
	v_mov_b32_e32 v34, 0
	v_mov_b32_e32 v35, v147
	v_mov_b32_e32 v36, v147
	v_mov_b32_e32 v37, v147
	v_mov_b32_e32 v38, 0
	v_mov_b32_e32 v39, v147
	v_mov_b32_e32 v40, v147
	v_mov_b32_e32 v41, v147
	v_mov_b32_e32 v46, 0
	v_mov_b32_e32 v47, v147
	v_mov_b32_e32 v48, v147
	v_mov_b32_e32 v49, v147
	v_mov_b32_e32 v62, 0
	v_mov_b32_e32 v63, v147
	v_mov_b32_e32 v64, v147
	v_mov_b32_e32 v65, v147
	v_mov_b32_e32 v66, 0
	v_mov_b32_e32 v67, v147
	v_mov_b32_e32 v68, v147
	v_mov_b32_e32 v69, v147
	v_mov_b32_e32 v78, 0
	v_mov_b32_e32 v79, v147
	v_mov_b32_e32 v80, v147
	v_mov_b32_e32 v81, v147
	v_mov_b32_e32 v90, 0
	v_mov_b32_e32 v91, v147
	v_mov_b32_e32 v92, v147
	v_mov_b32_e32 v93, v147
	v_mov_b32_e32 v94, 0
	v_mov_b32_e32 v95, v147
	v_mov_b32_e32 v96, v147
	v_mov_b32_e32 v97, v147
	v_mov_b32_e32 v114, 0
	v_mov_b32_e32 v115, v147
	v_mov_b32_e32 v116, v147
	v_mov_b32_e32 v117, v147
	v_mov_b32_e32 v122, 0
	v_mov_b32_e32 v123, v147
	v_mov_b32_e32 v124, v147
	v_mov_b32_e32 v125, v147
	v_mov_b32_e32 v138, 0
	v_mov_b32_e32 v139, v147
	v_mov_b32_e32 v140, v147
	v_mov_b32_e32 v141, v147
	v_mov_b32_e32 v142, 0
	v_mov_b32_e32 v143, v147
	v_mov_b32_e32 v144, v147
	v_mov_b32_e32 v145, v147
	v_mov_b32_e32 v118, 0
	v_mov_b32_e32 v119, v147
	v_mov_b32_e32 v120, v147
	v_mov_b32_e32 v121, v147
	v_mov_b32_e32 v126, 0
	v_mov_b32_e32 v127, v147
	v_mov_b32_e32 v128, v147
	v_mov_b32_e32 v129, v147
	v_mov_b32_e32 v134, 0
	v_mov_b32_e32 v135, v147
	v_mov_b32_e32 v136, v147
	v_mov_b32_e32 v137, v147
	v_mov_b32_e32 v130, 0
	v_mov_b32_e32 v131, v147
	v_mov_b32_e32 v132, v147
	v_mov_b32_e32 v133, v147
	v_mov_b32_e32 v98, 0
	v_mov_b32_e32 v99, v147
	v_mov_b32_e32 v100, v147
	v_mov_b32_e32 v101, v147
	v_mov_b32_e32 v102, 0
	v_mov_b32_e32 v103, v147
	v_mov_b32_e32 v104, v147
	v_mov_b32_e32 v105, v147
	v_mov_b32_e32 v110, 0
	v_mov_b32_e32 v111, v147
	v_mov_b32_e32 v112, v147
	v_mov_b32_e32 v113, v147
	v_mov_b32_e32 v106, 0
	v_mov_b32_e32 v107, v147
	v_mov_b32_e32 v108, v147
	v_mov_b32_e32 v109, v147
	v_mov_b32_e32 v70, 0
	v_mov_b32_e32 v71, v147
	v_mov_b32_e32 v72, v147
	v_mov_b32_e32 v73, v147
	v_mov_b32_e32 v82, 0
	v_mov_b32_e32 v83, v147
	v_mov_b32_e32 v84, v147
	v_mov_b32_e32 v85, v147
	v_mov_b32_e32 v86, 0
	v_mov_b32_e32 v87, v147
	v_mov_b32_e32 v88, v147
	v_mov_b32_e32 v89, v147
	v_mov_b32_e32 v74, 0
	v_mov_b32_e32 v75, v147
	v_mov_b32_e32 v76, v147
	v_mov_b32_e32 v77, v147
	v_mov_b32_e32 v42, 0
	v_mov_b32_e32 v43, v147
	v_mov_b32_e32 v44, v147
	v_mov_b32_e32 v45, v147
	v_mov_b32_e32 v54, 0
	v_mov_b32_e32 v55, v147
	v_mov_b32_e32 v56, v147
	v_mov_b32_e32 v57, v147
	v_mov_b32_e32 v58, 0
	v_mov_b32_e32 v59, v147
	v_mov_b32_e32 v60, v147
	v_mov_b32_e32 v61, v147
	v_mov_b32_e32 v50, 0
	v_mov_b32_e32 v51, v147
	v_mov_b32_e32 v52, v147
	v_mov_b32_e32 v53, v147
.LBB0_430:
	s_add_i32 s9, s6, 0xffff8000
	s_and_b32 s9, s9, 0x8000
	s_add_i32 s9, s9, 0
	s_add_i32 s8, s5, 0
	s_add_i32 s9, s9, 0x18000
	v_add_u32_e32 v204, s9, v153
	v_add_u32_e32 v206, s8, v169
	v_add_u32_e32 v212, s9, v151
	v_add_u32_e32 v208, s9, v152
	ds_read_b64_tr_b16 v[174:175], v204
	ds_read_b64_tr_b16 v[176:177], v204 offset:2048
	ds_read_b64_tr_b16 v[178:179], v208
	ds_read_b64_tr_b16 v[180:181], v208 offset:2048
	ds_read_b128 v[182:185], v206
	ds_read_b128 v[186:189], v206 offset:2048
	ds_read_b64_tr_b16 v[190:191], v212
	ds_read_b64_tr_b16 v[192:193], v212 offset:2048
	v_add_u32_e32 v214, s9, v146
	ds_read_b64_tr_b16 v[194:195], v214
	ds_read_b64_tr_b16 v[196:197], v214 offset:2048
	ds_read_b128 v[198:201], v206 offset:4096
	s_waitcnt lgkmcnt(6)
	v_mfma_f32_16x16x32_bf16 v[62:65], v[174:177], v[182:185], v[62:65]
	v_add_u32_e32 v202, 0xfff40000, v173
	s_add_i32 s9, s2, s7
	s_mov_b32 s14, m0
	s_mov_b32 m0, s9
	s_nop 0
	global_load_lds_dwordx4 v202, s[16:17]
	s_mov_b32 m0, s14
	v_mfma_f32_16x16x32_bf16 v[46:49], v[178:181], v[182:185], v[46:49]
	s_waitcnt lgkmcnt(3)
	v_mfma_f32_16x16x32_bf16 v[38:41], v[190:193], v[182:185], v[38:41]
	s_waitcnt lgkmcnt(1)
	v_mfma_f32_16x16x32_bf16 v[34:37], v[194:197], v[182:185], v[34:37]
	v_mfma_f32_16x16x32_bf16 v[30:33], v[174:177], v[186:189], v[30:33]
	ds_read_b128 v[182:185], v206 offset:6144
	v_add_u32_e32 v202, 0xfff80000, v173
	s_add_i32 s14, s9, 0x2000
	v_mfma_f32_16x16x32_bf16 v[26:29], v[178:181], v[186:189], v[26:29]
	s_mov_b32 s30, m0
	s_mov_b32 m0, s14
	s_nop 0
	global_load_lds_dwordx4 v202, s[16:17]
	s_mov_b32 m0, s30
	v_mfma_f32_16x16x32_bf16 v[22:25], v[190:193], v[186:189], v[22:25]
	v_mfma_f32_16x16x32_bf16 v[18:21], v[194:197], v[186:189], v[18:21]
	s_waitcnt lgkmcnt(1)
	v_mfma_f32_16x16x32_bf16 v[66:69], v[174:177], v[198:201], v[66:69]
	ds_read_b128 v[186:189], v206 offset:8192
	v_add_u32_e32 v202, 0xfffc0000, v173
	s_add_i32 s14, s9, 0x4000
	v_mfma_f32_16x16x32_bf16 v[78:81], v[178:181], v[198:201], v[78:81]
	s_mov_b32 s30, m0
	s_mov_b32 m0, s14
	s_nop 0
	global_load_lds_dwordx4 v202, s[16:17]
	s_mov_b32 m0, s30
	v_mfma_f32_16x16x32_bf16 v[90:93], v[190:193], v[198:201], v[90:93]
	v_mfma_f32_16x16x32_bf16 v[94:97], v[194:197], v[198:201], v[94:97]
	s_waitcnt lgkmcnt(1)
	v_mfma_f32_16x16x32_bf16 v[114:117], v[174:177], v[182:185], v[114:117]
	ds_read_b128 v[198:201], v206 offset:10240
	s_addk_i32 s9, 0x6000
	s_mov_b32 s14, m0
	s_mov_b32 m0, s9
	s_nop 0
	global_load_lds_dwordx4 v173, s[16:17]
	s_mov_b32 m0, s14
	v_mfma_f32_16x16x32_bf16 v[122:125], v[178:181], v[182:185], v[122:125]
	v_mfma_f32_16x16x32_bf16 v[138:141], v[190:193], v[182:185], v[138:141]
	v_mfma_f32_16x16x32_bf16 v[142:145], v[194:197], v[182:185], v[142:145]
	ds_read_b128 v[182:185], v206 offset:12288
	ds_read_b64_tr_b16 v[202:203], v204 offset:16384
	ds_read_b64_tr_b16 v[204:205], v204 offset:18432
	s_waitcnt lgkmcnt(4)
	v_mfma_f32_16x16x32_bf16 v[118:121], v[174:177], v[186:189], v[118:121]
	v_mfma_f32_16x16x32_bf16 v[126:129], v[178:181], v[186:189], v[126:129]
	v_mfma_f32_16x16x32_bf16 v[134:137], v[190:193], v[186:189], v[134:137]
	v_mfma_f32_16x16x32_bf16 v[130:133], v[194:197], v[186:189], v[130:133]
	ds_read_b128 v[186:189], v206 offset:14336
	ds_read_b64_tr_b16 v[206:207], v208 offset:16384
	ds_read_b64_tr_b16 v[208:209], v208 offset:18432
	s_waitcnt lgkmcnt(6)
	v_mfma_f32_16x16x32_bf16 v[98:101], v[174:177], v[198:201], v[98:101]
	v_mfma_f32_16x16x32_bf16 v[102:105], v[178:181], v[198:201], v[102:105]
	v_mfma_f32_16x16x32_bf16 v[110:113], v[190:193], v[198:201], v[110:113]
	v_mfma_f32_16x16x32_bf16 v[106:109], v[194:197], v[198:201], v[106:109]
	v_add_u32_e32 v215, s8, v171
	ds_read_b128 v[198:201], v215
	ds_read_b64_tr_b16 v[210:211], v212 offset:16384
	ds_read_b64_tr_b16 v[212:213], v212 offset:18432
	s_waitcnt lgkmcnt(8)
	v_mfma_f32_16x16x32_bf16 v[70:73], v[174:177], v[182:185], v[70:73]
	v_mfma_f32_16x16x32_bf16 v[82:85], v[178:181], v[182:185], v[82:85]
	v_mfma_f32_16x16x32_bf16 v[86:89], v[190:193], v[182:185], v[86:89]
	v_mfma_f32_16x16x32_bf16 v[74:77], v[194:197], v[182:185], v[74:77]
	s_waitcnt lgkmcnt(5)
	v_mfma_f32_16x16x32_bf16 v[42:45], v[174:177], v[186:189], v[42:45]
	ds_read_b128 v[174:177], v215 offset:2048
	s_and_b32 s8, s6, 0x8000
	v_mfma_f32_16x16x32_bf16 v[54:57], v[178:181], v[186:189], v[54:57]
	ds_read_b64_tr_b16 v[178:179], v214 offset:16384
	ds_read_b64_tr_b16 v[180:181], v214 offset:18432
	v_mfma_f32_16x16x32_bf16 v[58:61], v[190:193], v[186:189], v[58:61]
	v_mfma_f32_16x16x32_bf16 v[50:53], v[194:197], v[186:189], v[50:53]
	s_waitcnt lgkmcnt(5)
	v_mfma_f32_16x16x32_bf16 v[62:65], v[202:205], v[198:201], v[62:65]
	ds_read_b128 v[182:185], v215 offset:4096
	s_add_u32 s14, s3, s0
	s_addc_u32 s30, s4, s1
	v_mfma_f32_16x16x32_bf16 v[46:49], v[206:209], v[198:201], v[46:49]
	s_waitcnt vmcnt(15)
	v_add_u32_e32 v190, s8, v172
	s_add_u32 s8, s14, 0x180000
	s_waitcnt lgkmcnt(4)
	v_mfma_f32_16x16x32_bf16 v[38:41], v[210:213], v[198:201], v[38:41]
	ds_write_b128 v190, v[14:17]
	s_addc_u32 s9, s30, 0
	global_load_dwordx4 v[14:17], v162, s[8:9]
	s_waitcnt lgkmcnt(2)
	v_mfma_f32_16x16x32_bf16 v[34:37], v[178:181], v[198:201], v[34:37]
	v_mfma_f32_16x16x32_bf16 v[30:33], v[202:205], v[174:177], v[30:33]
	ds_read_b128 v[186:189], v215 offset:6144
	s_waitcnt vmcnt(15)
	s_add_u32 s8, s14, 0x1a0000
	v_mfma_f32_16x16x32_bf16 v[26:29], v[206:209], v[174:177], v[26:29]
	ds_write_b128 v190, v[10:13] offset:8192
	s_addc_u32 s9, s30, 0
	global_load_dwordx4 v[10:13], v162, s[8:9]
	v_mfma_f32_16x16x32_bf16 v[22:25], v[210:213], v[174:177], v[22:25]
	v_mfma_f32_16x16x32_bf16 v[18:21], v[178:181], v[174:177], v[18:21]
	s_waitcnt lgkmcnt(3)
	v_mfma_f32_16x16x32_bf16 v[66:69], v[202:205], v[182:185], v[66:69]
	ds_read_b128 v[174:177], v215 offset:8192
	s_waitcnt vmcnt(15)
	s_add_u32 s8, s14, 0x1c0000
	v_mfma_f32_16x16x32_bf16 v[78:81], v[206:209], v[182:185], v[78:81]
	ds_write_b128 v190, v[6:9] offset:16384
	s_addc_u32 s9, s30, 0
	global_load_dwordx4 v[6:9], v162, s[8:9]
	v_mfma_f32_16x16x32_bf16 v[90:93], v[210:213], v[182:185], v[90:93]
	v_mfma_f32_16x16x32_bf16 v[94:97], v[178:181], v[182:185], v[94:97]
	s_waitcnt lgkmcnt(3)
	v_mfma_f32_16x16x32_bf16 v[114:117], v[202:205], v[186:189], v[114:117]
	ds_read_b128 v[182:185], v215 offset:10240
	s_waitcnt vmcnt(15)
	s_add_u32 s8, s14, 0x1e0000
	v_mfma_f32_16x16x32_bf16 v[122:125], v[206:209], v[186:189], v[122:125]
	ds_write_b128 v190, v[2:5] offset:24576
	s_addc_u32 s9, s30, 0
	global_load_dwordx4 v[2:5], v162, s[8:9]
	v_mfma_f32_16x16x32_bf16 v[138:141], v[210:213], v[186:189], v[138:141]
	v_mfma_f32_16x16x32_bf16 v[142:145], v[178:181], v[186:189], v[142:145]
	s_waitcnt lgkmcnt(3)
	v_mfma_f32_16x16x32_bf16 v[118:121], v[202:205], v[174:177], v[118:121]
	ds_read_b128 v[186:189], v215 offset:12288
	v_mfma_f32_16x16x32_bf16 v[126:129], v[206:209], v[174:177], v[126:129]
	v_mfma_f32_16x16x32_bf16 v[134:137], v[210:213], v[174:177], v[134:137]
	v_mfma_f32_16x16x32_bf16 v[130:133], v[178:181], v[174:177], v[130:133]
	s_waitcnt lgkmcnt(2)
	v_mfma_f32_16x16x32_bf16 v[98:101], v[202:205], v[182:185], v[98:101]
	ds_read_b128 v[174:177], v215 offset:14336
	v_mfma_f32_16x16x32_bf16 v[102:105], v[206:209], v[182:185], v[102:105]
	v_mfma_f32_16x16x32_bf16 v[110:113], v[210:213], v[182:185], v[110:113]
	v_mfma_f32_16x16x32_bf16 v[106:109], v[178:181], v[182:185], v[106:109]
	s_waitcnt lgkmcnt(1)
	v_mfma_f32_16x16x32_bf16 v[70:73], v[202:205], v[186:189], v[70:73]
	v_mfma_f32_16x16x32_bf16 v[82:85], v[206:209], v[186:189], v[82:85]
	v_mfma_f32_16x16x32_bf16 v[86:89], v[210:213], v[186:189], v[86:89]
	v_mfma_f32_16x16x32_bf16 v[74:77], v[178:181], v[186:189], v[74:77]
	s_waitcnt lgkmcnt(0)
	v_mfma_f32_16x16x32_bf16 v[42:45], v[202:205], v[174:177], v[42:45]
	v_mfma_f32_16x16x32_bf16 v[54:57], v[206:209], v[174:177], v[54:57]
	v_mfma_f32_16x16x32_bf16 v[58:61], v[210:213], v[174:177], v[58:61]
	v_mfma_f32_16x16x32_bf16 v[50:53], v[178:181], v[174:177], v[50:53]
	s_add_i32 s8, s5, 0x8000
	s_cmp_lg_u32 s5, 0x10000
	s_cselect_b32 s5, s8, 0
	s_add_i32 s8, s7, 0x8000
	s_cmp_lg_u32 s7, 0x10000
	s_waitcnt vmcnt(12)
	s_waitcnt lgkmcnt(0)
	s_barrier
	s_cselect_b32 s7, s8, 0
	s_add_u32 s0, s0, 0x80000
	s_addc_u32 s1, s1, 0
	s_add_i32 s6, s6, 0x8000
	v_add_u32_e32 v173, 0x80, v173
	s_add_i32 s9, s6, 0xffff8000
	s_and_b32 s9, s9, 0x8000
	s_add_i32 s9, s9, 0
	s_add_i32 s8, s5, 0
	s_add_i32 s9, s9, 0x18000
	v_add_u32_e32 v204, s9, v153
	v_add_u32_e32 v206, s8, v169
	v_add_u32_e32 v212, s9, v151
	v_add_u32_e32 v208, s9, v152
	ds_read_b64_tr_b16 v[174:175], v204
	ds_read_b64_tr_b16 v[176:177], v204 offset:2048
	ds_read_b64_tr_b16 v[178:179], v208
	ds_read_b64_tr_b16 v[180:181], v208 offset:2048
	ds_read_b128 v[182:185], v206
	ds_read_b128 v[186:189], v206 offset:2048
	ds_read_b64_tr_b16 v[190:191], v212
	ds_read_b64_tr_b16 v[192:193], v212 offset:2048
	v_add_u32_e32 v214, s9, v146
	ds_read_b64_tr_b16 v[194:195], v214
	ds_read_b64_tr_b16 v[196:197], v214 offset:2048
	ds_read_b128 v[198:201], v206 offset:4096
	s_waitcnt lgkmcnt(6)
	v_mfma_f32_16x16x32_bf16 v[62:65], v[174:177], v[182:185], v[62:65]
	v_add_u32_e32 v202, 0xfff40000, v173
	s_add_i32 s9, s2, s7
	s_mov_b32 s14, m0
	s_mov_b32 m0, s9
	s_nop 0
	global_load_lds_dwordx4 v202, s[16:17]
	s_mov_b32 m0, s14
	v_mfma_f32_16x16x32_bf16 v[46:49], v[178:181], v[182:185], v[46:49]
	s_waitcnt lgkmcnt(3)
	v_mfma_f32_16x16x32_bf16 v[38:41], v[190:193], v[182:185], v[38:41]
	s_waitcnt lgkmcnt(1)
	v_mfma_f32_16x16x32_bf16 v[34:37], v[194:197], v[182:185], v[34:37]
	v_mfma_f32_16x16x32_bf16 v[30:33], v[174:177], v[186:189], v[30:33]
	ds_read_b128 v[182:185], v206 offset:6144
	v_add_u32_e32 v202, 0xfff80000, v173
	s_add_i32 s14, s9, 0x2000
	v_mfma_f32_16x16x32_bf16 v[26:29], v[178:181], v[186:189], v[26:29]
	s_mov_b32 s30, m0
	s_mov_b32 m0, s14
	s_nop 0
	global_load_lds_dwordx4 v202, s[16:17]
	s_mov_b32 m0, s30
	v_mfma_f32_16x16x32_bf16 v[22:25], v[190:193], v[186:189], v[22:25]
	v_mfma_f32_16x16x32_bf16 v[18:21], v[194:197], v[186:189], v[18:21]
	s_waitcnt lgkmcnt(1)
	v_mfma_f32_16x16x32_bf16 v[66:69], v[174:177], v[198:201], v[66:69]
	ds_read_b128 v[186:189], v206 offset:8192
	v_add_u32_e32 v202, 0xfffc0000, v173
	s_add_i32 s14, s9, 0x4000
	v_mfma_f32_16x16x32_bf16 v[78:81], v[178:181], v[198:201], v[78:81]
	s_mov_b32 s30, m0
	s_mov_b32 m0, s14
	s_nop 0
	global_load_lds_dwordx4 v202, s[16:17]
	s_mov_b32 m0, s30
	v_mfma_f32_16x16x32_bf16 v[90:93], v[190:193], v[198:201], v[90:93]
	v_mfma_f32_16x16x32_bf16 v[94:97], v[194:197], v[198:201], v[94:97]
	s_waitcnt lgkmcnt(1)
	v_mfma_f32_16x16x32_bf16 v[114:117], v[174:177], v[182:185], v[114:117]
	ds_read_b128 v[198:201], v206 offset:10240
	s_addk_i32 s9, 0x6000
	s_mov_b32 s14, m0
	s_mov_b32 m0, s9
	s_nop 0
	global_load_lds_dwordx4 v173, s[16:17]
	s_mov_b32 m0, s14
	v_mfma_f32_16x16x32_bf16 v[122:125], v[178:181], v[182:185], v[122:125]
	v_mfma_f32_16x16x32_bf16 v[138:141], v[190:193], v[182:185], v[138:141]
	v_mfma_f32_16x16x32_bf16 v[142:145], v[194:197], v[182:185], v[142:145]
	ds_read_b128 v[182:185], v206 offset:12288
	ds_read_b64_tr_b16 v[202:203], v204 offset:16384
	ds_read_b64_tr_b16 v[204:205], v204 offset:18432
	s_waitcnt lgkmcnt(4)
	v_mfma_f32_16x16x32_bf16 v[118:121], v[174:177], v[186:189], v[118:121]
	v_mfma_f32_16x16x32_bf16 v[126:129], v[178:181], v[186:189], v[126:129]
	v_mfma_f32_16x16x32_bf16 v[134:137], v[190:193], v[186:189], v[134:137]
	v_mfma_f32_16x16x32_bf16 v[130:133], v[194:197], v[186:189], v[130:133]
	ds_read_b128 v[186:189], v206 offset:14336
	ds_read_b64_tr_b16 v[206:207], v208 offset:16384
	ds_read_b64_tr_b16 v[208:209], v208 offset:18432
	s_waitcnt lgkmcnt(6)
	v_mfma_f32_16x16x32_bf16 v[98:101], v[174:177], v[198:201], v[98:101]
	v_mfma_f32_16x16x32_bf16 v[102:105], v[178:181], v[198:201], v[102:105]
	v_mfma_f32_16x16x32_bf16 v[110:113], v[190:193], v[198:201], v[110:113]
	v_mfma_f32_16x16x32_bf16 v[106:109], v[194:197], v[198:201], v[106:109]
	v_add_u32_e32 v215, s8, v171
	ds_read_b128 v[198:201], v215
	ds_read_b64_tr_b16 v[210:211], v212 offset:16384
	ds_read_b64_tr_b16 v[212:213], v212 offset:18432
	s_waitcnt lgkmcnt(8)
	v_mfma_f32_16x16x32_bf16 v[70:73], v[174:177], v[182:185], v[70:73]
	v_mfma_f32_16x16x32_bf16 v[82:85], v[178:181], v[182:185], v[82:85]
	v_mfma_f32_16x16x32_bf16 v[86:89], v[190:193], v[182:185], v[86:89]
	v_mfma_f32_16x16x32_bf16 v[74:77], v[194:197], v[182:185], v[74:77]
	s_waitcnt lgkmcnt(5)
	v_mfma_f32_16x16x32_bf16 v[42:45], v[174:177], v[186:189], v[42:45]
	ds_read_b128 v[174:177], v215 offset:2048
	s_and_b32 s8, s6, 0x8000
	v_mfma_f32_16x16x32_bf16 v[54:57], v[178:181], v[186:189], v[54:57]
	ds_read_b64_tr_b16 v[178:179], v214 offset:16384
	ds_read_b64_tr_b16 v[180:181], v214 offset:18432
	v_mfma_f32_16x16x32_bf16 v[58:61], v[190:193], v[186:189], v[58:61]
	v_mfma_f32_16x16x32_bf16 v[50:53], v[194:197], v[186:189], v[50:53]
	s_waitcnt lgkmcnt(5)
	v_mfma_f32_16x16x32_bf16 v[62:65], v[202:205], v[198:201], v[62:65]
	ds_read_b128 v[182:185], v215 offset:4096
	s_add_u32 s14, s3, s0
	s_addc_u32 s30, s4, s1
	v_mfma_f32_16x16x32_bf16 v[46:49], v[206:209], v[198:201], v[46:49]
	s_waitcnt vmcnt(15)
	v_add_u32_e32 v190, s8, v172
	s_add_u32 s8, s14, 0x180000
	s_waitcnt lgkmcnt(4)
	v_mfma_f32_16x16x32_bf16 v[38:41], v[210:213], v[198:201], v[38:41]
	ds_write_b128 v190, v[228:231]
	s_addc_u32 s9, s30, 0
	global_load_dwordx4 v[228:231], v162, s[8:9]
	s_waitcnt lgkmcnt(2)
	v_mfma_f32_16x16x32_bf16 v[34:37], v[178:181], v[198:201], v[34:37]
	v_mfma_f32_16x16x32_bf16 v[30:33], v[202:205], v[174:177], v[30:33]
	ds_read_b128 v[186:189], v215 offset:6144
	s_waitcnt vmcnt(15)
	s_add_u32 s8, s14, 0x1a0000
	v_mfma_f32_16x16x32_bf16 v[26:29], v[206:209], v[174:177], v[26:29]
	ds_write_b128 v190, v[224:227] offset:8192
	s_addc_u32 s9, s30, 0
	global_load_dwordx4 v[224:227], v162, s[8:9]
	v_mfma_f32_16x16x32_bf16 v[22:25], v[210:213], v[174:177], v[22:25]
	v_mfma_f32_16x16x32_bf16 v[18:21], v[178:181], v[174:177], v[18:21]
	s_waitcnt lgkmcnt(3)
	v_mfma_f32_16x16x32_bf16 v[66:69], v[202:205], v[182:185], v[66:69]
	ds_read_b128 v[174:177], v215 offset:8192
	s_waitcnt vmcnt(15)
	s_add_u32 s8, s14, 0x1c0000
	v_mfma_f32_16x16x32_bf16 v[78:81], v[206:209], v[182:185], v[78:81]
	ds_write_b128 v190, v[220:223] offset:16384
	s_addc_u32 s9, s30, 0
	global_load_dwordx4 v[220:223], v162, s[8:9]
	v_mfma_f32_16x16x32_bf16 v[90:93], v[210:213], v[182:185], v[90:93]
	v_mfma_f32_16x16x32_bf16 v[94:97], v[178:181], v[182:185], v[94:97]
	s_waitcnt lgkmcnt(3)
	v_mfma_f32_16x16x32_bf16 v[114:117], v[202:205], v[186:189], v[114:117]
	ds_read_b128 v[182:185], v215 offset:10240
	s_waitcnt vmcnt(15)
	s_add_u32 s8, s14, 0x1e0000
	v_mfma_f32_16x16x32_bf16 v[122:125], v[206:209], v[186:189], v[122:125]
	ds_write_b128 v190, v[216:219] offset:24576
	s_addc_u32 s9, s30, 0
	global_load_dwordx4 v[216:219], v162, s[8:9]
	v_mfma_f32_16x16x32_bf16 v[138:141], v[210:213], v[186:189], v[138:141]
	v_mfma_f32_16x16x32_bf16 v[142:145], v[178:181], v[186:189], v[142:145]
	s_waitcnt lgkmcnt(3)
	v_mfma_f32_16x16x32_bf16 v[118:121], v[202:205], v[174:177], v[118:121]
	ds_read_b128 v[186:189], v215 offset:12288
	v_mfma_f32_16x16x32_bf16 v[126:129], v[206:209], v[174:177], v[126:129]
	v_mfma_f32_16x16x32_bf16 v[134:137], v[210:213], v[174:177], v[134:137]
	v_mfma_f32_16x16x32_bf16 v[130:133], v[178:181], v[174:177], v[130:133]
	s_waitcnt lgkmcnt(2)
	v_mfma_f32_16x16x32_bf16 v[98:101], v[202:205], v[182:185], v[98:101]
	ds_read_b128 v[174:177], v215 offset:14336
	v_mfma_f32_16x16x32_bf16 v[102:105], v[206:209], v[182:185], v[102:105]
	v_mfma_f32_16x16x32_bf16 v[110:113], v[210:213], v[182:185], v[110:113]
	v_mfma_f32_16x16x32_bf16 v[106:109], v[178:181], v[182:185], v[106:109]
	s_waitcnt lgkmcnt(1)
	v_mfma_f32_16x16x32_bf16 v[70:73], v[202:205], v[186:189], v[70:73]
	v_mfma_f32_16x16x32_bf16 v[82:85], v[206:209], v[186:189], v[82:85]
	v_mfma_f32_16x16x32_bf16 v[86:89], v[210:213], v[186:189], v[86:89]
	v_mfma_f32_16x16x32_bf16 v[74:77], v[178:181], v[186:189], v[74:77]
	s_waitcnt lgkmcnt(0)
	v_mfma_f32_16x16x32_bf16 v[42:45], v[202:205], v[174:177], v[42:45]
	v_mfma_f32_16x16x32_bf16 v[54:57], v[206:209], v[174:177], v[54:57]
	v_mfma_f32_16x16x32_bf16 v[58:61], v[210:213], v[174:177], v[58:61]
	v_mfma_f32_16x16x32_bf16 v[50:53], v[178:181], v[174:177], v[50:53]
	s_add_i32 s8, s5, 0x8000
	s_cmp_lg_u32 s5, 0x10000
	s_cselect_b32 s5, s8, 0
	s_add_i32 s8, s7, 0x8000
	s_cmp_lg_u32 s7, 0x10000
	s_waitcnt vmcnt(12)
	s_waitcnt lgkmcnt(0)
	s_barrier
	s_cselect_b32 s7, s8, 0
	s_add_u32 s0, s0, 0x80000
	s_addc_u32 s1, s1, 0
	s_add_i32 s6, s6, 0x8000
	s_cmp_lg_u32 s0, 0xe00000
	v_add_u32_e32 v173, 0x80, v173
	s_cbranch_scc1 .LBB0_430
	s_add_i32 s9, s6, 0xffff8000
	s_and_b32 s9, s9, 0x8000
	s_add_i32 s9, s9, 0
	s_add_i32 s8, s5, 0
	s_add_i32 s9, s9, 0x18000
	v_add_u32_e32 v204, s9, v153
	v_add_u32_e32 v206, s8, v169
	v_add_u32_e32 v212, s9, v151
	v_add_u32_e32 v208, s9, v152
	ds_read_b64_tr_b16 v[174:175], v204
	ds_read_b64_tr_b16 v[176:177], v204 offset:2048
	ds_read_b64_tr_b16 v[178:179], v208
	ds_read_b64_tr_b16 v[180:181], v208 offset:2048
	ds_read_b128 v[182:185], v206
	ds_read_b128 v[186:189], v206 offset:2048
	ds_read_b64_tr_b16 v[190:191], v212
	ds_read_b64_tr_b16 v[192:193], v212 offset:2048
	v_add_u32_e32 v214, s9, v146
	ds_read_b64_tr_b16 v[194:195], v214
	ds_read_b64_tr_b16 v[196:197], v214 offset:2048
	ds_read_b128 v[198:201], v206 offset:4096
	s_waitcnt lgkmcnt(6)
	v_mfma_f32_16x16x32_bf16 v[62:65], v[174:177], v[182:185], v[62:65]
	v_add_u32_e32 v202, 0xfff40000, v173
	s_add_i32 s9, s2, s7
	s_mov_b32 s14, m0
	s_mov_b32 m0, s9
	s_nop 0
	global_load_lds_dwordx4 v202, s[16:17]
	s_mov_b32 m0, s14
	v_mfma_f32_16x16x32_bf16 v[46:49], v[178:181], v[182:185], v[46:49]
	s_waitcnt lgkmcnt(3)
	v_mfma_f32_16x16x32_bf16 v[38:41], v[190:193], v[182:185], v[38:41]
	s_waitcnt lgkmcnt(1)
	v_mfma_f32_16x16x32_bf16 v[34:37], v[194:197], v[182:185], v[34:37]
	v_mfma_f32_16x16x32_bf16 v[30:33], v[174:177], v[186:189], v[30:33]
	ds_read_b128 v[182:185], v206 offset:6144
	v_add_u32_e32 v202, 0xfff80000, v173
	s_add_i32 s14, s9, 0x2000
	v_mfma_f32_16x16x32_bf16 v[26:29], v[178:181], v[186:189], v[26:29]
	s_mov_b32 s30, m0
	s_mov_b32 m0, s14
	s_nop 0
	global_load_lds_dwordx4 v202, s[16:17]
	s_mov_b32 m0, s30
	v_mfma_f32_16x16x32_bf16 v[22:25], v[190:193], v[186:189], v[22:25]
	v_mfma_f32_16x16x32_bf16 v[18:21], v[194:197], v[186:189], v[18:21]
	s_waitcnt lgkmcnt(1)
	v_mfma_f32_16x16x32_bf16 v[66:69], v[174:177], v[198:201], v[66:69]
	ds_read_b128 v[186:189], v206 offset:8192
	v_add_u32_e32 v202, 0xfffc0000, v173
	s_add_i32 s14, s9, 0x4000
	v_mfma_f32_16x16x32_bf16 v[78:81], v[178:181], v[198:201], v[78:81]
	s_mov_b32 s30, m0
	s_mov_b32 m0, s14
	s_nop 0
	global_load_lds_dwordx4 v202, s[16:17]
	s_mov_b32 m0, s30
	v_mfma_f32_16x16x32_bf16 v[90:93], v[190:193], v[198:201], v[90:93]
	v_mfma_f32_16x16x32_bf16 v[94:97], v[194:197], v[198:201], v[94:97]
	s_waitcnt lgkmcnt(1)
	v_mfma_f32_16x16x32_bf16 v[114:117], v[174:177], v[182:185], v[114:117]
	ds_read_b128 v[198:201], v206 offset:10240
	s_addk_i32 s9, 0x6000
	s_mov_b32 s14, m0
	s_mov_b32 m0, s9
	s_nop 0
	global_load_lds_dwordx4 v173, s[16:17]
	s_mov_b32 m0, s14
	v_mfma_f32_16x16x32_bf16 v[122:125], v[178:181], v[182:185], v[122:125]
	v_mfma_f32_16x16x32_bf16 v[138:141], v[190:193], v[182:185], v[138:141]
	v_mfma_f32_16x16x32_bf16 v[142:145], v[194:197], v[182:185], v[142:145]
	ds_read_b128 v[182:185], v206 offset:12288
	ds_read_b64_tr_b16 v[202:203], v204 offset:16384
	ds_read_b64_tr_b16 v[204:205], v204 offset:18432
	s_waitcnt lgkmcnt(4)
	v_mfma_f32_16x16x32_bf16 v[118:121], v[174:177], v[186:189], v[118:121]
	v_mfma_f32_16x16x32_bf16 v[126:129], v[178:181], v[186:189], v[126:129]
	v_mfma_f32_16x16x32_bf16 v[134:137], v[190:193], v[186:189], v[134:137]
	v_mfma_f32_16x16x32_bf16 v[130:133], v[194:197], v[186:189], v[130:133]
	ds_read_b128 v[186:189], v206 offset:14336
	ds_read_b64_tr_b16 v[206:207], v208 offset:16384
	ds_read_b64_tr_b16 v[208:209], v208 offset:18432
	s_waitcnt lgkmcnt(6)
	v_mfma_f32_16x16x32_bf16 v[98:101], v[174:177], v[198:201], v[98:101]
	v_mfma_f32_16x16x32_bf16 v[102:105], v[178:181], v[198:201], v[102:105]
	v_mfma_f32_16x16x32_bf16 v[110:113], v[190:193], v[198:201], v[110:113]
	v_mfma_f32_16x16x32_bf16 v[106:109], v[194:197], v[198:201], v[106:109]
	v_add_u32_e32 v215, s8, v171
	ds_read_b128 v[198:201], v215
	ds_read_b64_tr_b16 v[210:211], v212 offset:16384
	ds_read_b64_tr_b16 v[212:213], v212 offset:18432
	s_waitcnt lgkmcnt(8)
	v_mfma_f32_16x16x32_bf16 v[70:73], v[174:177], v[182:185], v[70:73]
	v_mfma_f32_16x16x32_bf16 v[82:85], v[178:181], v[182:185], v[82:85]
	v_mfma_f32_16x16x32_bf16 v[86:89], v[190:193], v[182:185], v[86:89]
	v_mfma_f32_16x16x32_bf16 v[74:77], v[194:197], v[182:185], v[74:77]
	s_waitcnt lgkmcnt(5)
	v_mfma_f32_16x16x32_bf16 v[42:45], v[174:177], v[186:189], v[42:45]
	ds_read_b128 v[174:177], v215 offset:2048
	s_and_b32 s8, s6, 0x8000
	v_mfma_f32_16x16x32_bf16 v[54:57], v[178:181], v[186:189], v[54:57]
	ds_read_b64_tr_b16 v[178:179], v214 offset:16384
	ds_read_b64_tr_b16 v[180:181], v214 offset:18432
	v_mfma_f32_16x16x32_bf16 v[58:61], v[190:193], v[186:189], v[58:61]
	v_mfma_f32_16x16x32_bf16 v[50:53], v[194:197], v[186:189], v[50:53]
	s_waitcnt lgkmcnt(5)
	v_mfma_f32_16x16x32_bf16 v[62:65], v[202:205], v[198:201], v[62:65]
	ds_read_b128 v[182:185], v215 offset:4096
	s_add_u32 s14, s3, s0
	s_addc_u32 s30, s4, s1
	v_mfma_f32_16x16x32_bf16 v[46:49], v[206:209], v[198:201], v[46:49]
	s_waitcnt vmcnt(15)
	v_add_u32_e32 v190, s8, v172
	s_add_u32 s8, s14, 0x180000
	s_waitcnt lgkmcnt(4)
	v_mfma_f32_16x16x32_bf16 v[38:41], v[210:213], v[198:201], v[38:41]
	ds_write_b128 v190, v[14:17]
	s_addc_u32 s9, s30, 0
	global_load_dwordx4 v[14:17], v162, s[8:9]
	s_waitcnt lgkmcnt(2)
	v_mfma_f32_16x16x32_bf16 v[34:37], v[178:181], v[198:201], v[34:37]
	v_mfma_f32_16x16x32_bf16 v[30:33], v[202:205], v[174:177], v[30:33]
	ds_read_b128 v[186:189], v215 offset:6144
	s_waitcnt vmcnt(15)
	s_add_u32 s8, s14, 0x1a0000
	v_mfma_f32_16x16x32_bf16 v[26:29], v[206:209], v[174:177], v[26:29]
	ds_write_b128 v190, v[10:13] offset:8192
	s_addc_u32 s9, s30, 0
	global_load_dwordx4 v[10:13], v162, s[8:9]
	v_mfma_f32_16x16x32_bf16 v[22:25], v[210:213], v[174:177], v[22:25]
	v_mfma_f32_16x16x32_bf16 v[18:21], v[178:181], v[174:177], v[18:21]
	s_waitcnt lgkmcnt(3)
	v_mfma_f32_16x16x32_bf16 v[66:69], v[202:205], v[182:185], v[66:69]
	ds_read_b128 v[174:177], v215 offset:8192
	s_waitcnt vmcnt(15)
	s_add_u32 s8, s14, 0x1c0000
	v_mfma_f32_16x16x32_bf16 v[78:81], v[206:209], v[182:185], v[78:81]
	ds_write_b128 v190, v[6:9] offset:16384
	s_addc_u32 s9, s30, 0
	global_load_dwordx4 v[6:9], v162, s[8:9]
	v_mfma_f32_16x16x32_bf16 v[90:93], v[210:213], v[182:185], v[90:93]
	v_mfma_f32_16x16x32_bf16 v[94:97], v[178:181], v[182:185], v[94:97]
	s_waitcnt lgkmcnt(3)
	v_mfma_f32_16x16x32_bf16 v[114:117], v[202:205], v[186:189], v[114:117]
	ds_read_b128 v[182:185], v215 offset:10240
	s_waitcnt vmcnt(15)
	s_add_u32 s8, s14, 0x1e0000
	v_mfma_f32_16x16x32_bf16 v[122:125], v[206:209], v[186:189], v[122:125]
	ds_write_b128 v190, v[2:5] offset:24576
	s_addc_u32 s9, s30, 0
	global_load_dwordx4 v[2:5], v162, s[8:9]
	v_mfma_f32_16x16x32_bf16 v[138:141], v[210:213], v[186:189], v[138:141]
	v_mfma_f32_16x16x32_bf16 v[142:145], v[178:181], v[186:189], v[142:145]
	s_waitcnt lgkmcnt(3)
	v_mfma_f32_16x16x32_bf16 v[118:121], v[202:205], v[174:177], v[118:121]
	ds_read_b128 v[186:189], v215 offset:12288
	v_mfma_f32_16x16x32_bf16 v[126:129], v[206:209], v[174:177], v[126:129]
	v_mfma_f32_16x16x32_bf16 v[134:137], v[210:213], v[174:177], v[134:137]
	v_mfma_f32_16x16x32_bf16 v[130:133], v[178:181], v[174:177], v[130:133]
	s_waitcnt lgkmcnt(2)
	v_mfma_f32_16x16x32_bf16 v[98:101], v[202:205], v[182:185], v[98:101]
	ds_read_b128 v[174:177], v215 offset:14336
	v_mfma_f32_16x16x32_bf16 v[102:105], v[206:209], v[182:185], v[102:105]
	v_mfma_f32_16x16x32_bf16 v[110:113], v[210:213], v[182:185], v[110:113]
	v_mfma_f32_16x16x32_bf16 v[106:109], v[178:181], v[182:185], v[106:109]
	s_waitcnt lgkmcnt(1)
	v_mfma_f32_16x16x32_bf16 v[70:73], v[202:205], v[186:189], v[70:73]
	v_mfma_f32_16x16x32_bf16 v[82:85], v[206:209], v[186:189], v[82:85]
	v_mfma_f32_16x16x32_bf16 v[86:89], v[210:213], v[186:189], v[86:89]
	v_mfma_f32_16x16x32_bf16 v[74:77], v[178:181], v[186:189], v[74:77]
	s_waitcnt lgkmcnt(0)
	v_mfma_f32_16x16x32_bf16 v[42:45], v[202:205], v[174:177], v[42:45]
	v_mfma_f32_16x16x32_bf16 v[54:57], v[206:209], v[174:177], v[54:57]
	v_mfma_f32_16x16x32_bf16 v[58:61], v[210:213], v[174:177], v[58:61]
	v_mfma_f32_16x16x32_bf16 v[50:53], v[178:181], v[174:177], v[50:53]
	s_add_i32 s8, s5, 0x8000
	s_cmp_lg_u32 s5, 0x10000
	s_cselect_b32 s5, s8, 0
	s_add_i32 s8, s7, 0x8000
	s_cmp_lg_u32 s7, 0x10000
	s_waitcnt vmcnt(12)
	s_waitcnt lgkmcnt(0)
	s_barrier
	s_cselect_b32 s7, s8, 0
	s_add_u32 s0, s0, 0x80000
	s_addc_u32 s1, s1, 0
	s_add_i32 s6, s6, 0x8000
	v_add_u32_e32 v173, 0x80, v173
	s_add_i32 s9, s6, 0xffff8000
	s_and_b32 s9, s9, 0x8000
	s_add_i32 s9, s9, 0
	s_add_i32 s8, s5, 0
	s_add_i32 s9, s9, 0x18000
	v_add_u32_e32 v204, s9, v153
	v_add_u32_e32 v206, s8, v169
	v_add_u32_e32 v212, s9, v151
	v_add_u32_e32 v208, s9, v152
	ds_read_b64_tr_b16 v[174:175], v204
	ds_read_b64_tr_b16 v[176:177], v204 offset:2048
	ds_read_b64_tr_b16 v[178:179], v208
	ds_read_b64_tr_b16 v[180:181], v208 offset:2048
	ds_read_b128 v[182:185], v206
	ds_read_b128 v[186:189], v206 offset:2048
	ds_read_b64_tr_b16 v[190:191], v212
	ds_read_b64_tr_b16 v[192:193], v212 offset:2048
	v_add_u32_e32 v214, s9, v146
	ds_read_b64_tr_b16 v[194:195], v214
	ds_read_b64_tr_b16 v[196:197], v214 offset:2048
	ds_read_b128 v[198:201], v206 offset:4096
	s_waitcnt lgkmcnt(6)
	v_mfma_f32_16x16x32_bf16 v[62:65], v[174:177], v[182:185], v[62:65]
	v_add_u32_e32 v202, 0xfff40000, v173
	s_add_i32 s9, s2, s7
	s_mov_b32 s14, m0
	s_mov_b32 m0, s9
	s_nop 0
	global_load_lds_dwordx4 v202, s[16:17]
	s_mov_b32 m0, s14
	v_mfma_f32_16x16x32_bf16 v[46:49], v[178:181], v[182:185], v[46:49]
	s_waitcnt lgkmcnt(3)
	v_mfma_f32_16x16x32_bf16 v[38:41], v[190:193], v[182:185], v[38:41]
	s_waitcnt lgkmcnt(1)
	v_mfma_f32_16x16x32_bf16 v[34:37], v[194:197], v[182:185], v[34:37]
	v_mfma_f32_16x16x32_bf16 v[30:33], v[174:177], v[186:189], v[30:33]
	ds_read_b128 v[182:185], v206 offset:6144
	v_add_u32_e32 v202, 0xfff80000, v173
	s_add_i32 s14, s9, 0x2000
	v_mfma_f32_16x16x32_bf16 v[26:29], v[178:181], v[186:189], v[26:29]
	s_mov_b32 s30, m0
	s_mov_b32 m0, s14
	s_nop 0
	global_load_lds_dwordx4 v202, s[16:17]
	s_mov_b32 m0, s30
	v_mfma_f32_16x16x32_bf16 v[22:25], v[190:193], v[186:189], v[22:25]
	v_mfma_f32_16x16x32_bf16 v[18:21], v[194:197], v[186:189], v[18:21]
	s_waitcnt lgkmcnt(1)
	v_mfma_f32_16x16x32_bf16 v[66:69], v[174:177], v[198:201], v[66:69]
	ds_read_b128 v[186:189], v206 offset:8192
	v_add_u32_e32 v202, 0xfffc0000, v173
	s_add_i32 s14, s9, 0x4000
	v_mfma_f32_16x16x32_bf16 v[78:81], v[178:181], v[198:201], v[78:81]
	s_mov_b32 s30, m0
	s_mov_b32 m0, s14
	s_nop 0
	global_load_lds_dwordx4 v202, s[16:17]
	s_mov_b32 m0, s30
	v_mfma_f32_16x16x32_bf16 v[90:93], v[190:193], v[198:201], v[90:93]
	v_mfma_f32_16x16x32_bf16 v[94:97], v[194:197], v[198:201], v[94:97]
	s_waitcnt lgkmcnt(1)
	v_mfma_f32_16x16x32_bf16 v[114:117], v[174:177], v[182:185], v[114:117]
	ds_read_b128 v[198:201], v206 offset:10240
	s_addk_i32 s9, 0x6000
	s_mov_b32 s14, m0
	s_mov_b32 m0, s9
	s_nop 0
	global_load_lds_dwordx4 v173, s[16:17]
	s_mov_b32 m0, s14
	v_mfma_f32_16x16x32_bf16 v[122:125], v[178:181], v[182:185], v[122:125]
	v_mfma_f32_16x16x32_bf16 v[138:141], v[190:193], v[182:185], v[138:141]
	v_mfma_f32_16x16x32_bf16 v[142:145], v[194:197], v[182:185], v[142:145]
	ds_read_b128 v[182:185], v206 offset:12288
	ds_read_b64_tr_b16 v[202:203], v204 offset:16384
	ds_read_b64_tr_b16 v[204:205], v204 offset:18432
	s_waitcnt lgkmcnt(4)
	v_mfma_f32_16x16x32_bf16 v[118:121], v[174:177], v[186:189], v[118:121]
	v_mfma_f32_16x16x32_bf16 v[126:129], v[178:181], v[186:189], v[126:129]
	v_mfma_f32_16x16x32_bf16 v[134:137], v[190:193], v[186:189], v[134:137]
	v_mfma_f32_16x16x32_bf16 v[130:133], v[194:197], v[186:189], v[130:133]
	ds_read_b128 v[186:189], v206 offset:14336
	ds_read_b64_tr_b16 v[206:207], v208 offset:16384
	ds_read_b64_tr_b16 v[208:209], v208 offset:18432
	s_waitcnt lgkmcnt(6)
	v_mfma_f32_16x16x32_bf16 v[98:101], v[174:177], v[198:201], v[98:101]
	v_mfma_f32_16x16x32_bf16 v[102:105], v[178:181], v[198:201], v[102:105]
	v_mfma_f32_16x16x32_bf16 v[110:113], v[190:193], v[198:201], v[110:113]
	v_mfma_f32_16x16x32_bf16 v[106:109], v[194:197], v[198:201], v[106:109]
	v_add_u32_e32 v215, s8, v171
	ds_read_b128 v[198:201], v215
	ds_read_b64_tr_b16 v[210:211], v212 offset:16384
	ds_read_b64_tr_b16 v[212:213], v212 offset:18432
	s_waitcnt lgkmcnt(8)
	v_mfma_f32_16x16x32_bf16 v[70:73], v[174:177], v[182:185], v[70:73]
	v_mfma_f32_16x16x32_bf16 v[82:85], v[178:181], v[182:185], v[82:85]
	v_mfma_f32_16x16x32_bf16 v[86:89], v[190:193], v[182:185], v[86:89]
	v_mfma_f32_16x16x32_bf16 v[74:77], v[194:197], v[182:185], v[74:77]
	s_waitcnt lgkmcnt(5)
	v_mfma_f32_16x16x32_bf16 v[42:45], v[174:177], v[186:189], v[42:45]
	ds_read_b128 v[174:177], v215 offset:2048
	s_and_b32 s8, s6, 0x8000
	v_mfma_f32_16x16x32_bf16 v[54:57], v[178:181], v[186:189], v[54:57]
	ds_read_b64_tr_b16 v[178:179], v214 offset:16384
	ds_read_b64_tr_b16 v[180:181], v214 offset:18432
	v_mfma_f32_16x16x32_bf16 v[58:61], v[190:193], v[186:189], v[58:61]
	v_mfma_f32_16x16x32_bf16 v[50:53], v[194:197], v[186:189], v[50:53]
	s_waitcnt lgkmcnt(5)
	v_mfma_f32_16x16x32_bf16 v[62:65], v[202:205], v[198:201], v[62:65]
	ds_read_b128 v[182:185], v215 offset:4096
	s_add_u32 s14, s3, s0
	s_addc_u32 s30, s4, s1
	v_mfma_f32_16x16x32_bf16 v[46:49], v[206:209], v[198:201], v[46:49]
	s_waitcnt vmcnt(15)
	v_add_u32_e32 v190, s8, v172
	s_add_u32 s8, s14, 0x180000
	s_waitcnt lgkmcnt(4)
	v_mfma_f32_16x16x32_bf16 v[38:41], v[210:213], v[198:201], v[38:41]
	ds_write_b128 v190, v[228:231]
	s_addc_u32 s9, s30, 0
	s_waitcnt lgkmcnt(2)
	v_mfma_f32_16x16x32_bf16 v[34:37], v[178:181], v[198:201], v[34:37]
	v_mfma_f32_16x16x32_bf16 v[30:33], v[202:205], v[174:177], v[30:33]
	ds_read_b128 v[186:189], v215 offset:6144
	s_waitcnt vmcnt(14)
	s_add_u32 s8, s14, 0x1a0000
	v_mfma_f32_16x16x32_bf16 v[26:29], v[206:209], v[174:177], v[26:29]
	ds_write_b128 v190, v[224:227] offset:8192
	s_addc_u32 s9, s30, 0
	v_mfma_f32_16x16x32_bf16 v[22:25], v[210:213], v[174:177], v[22:25]
	v_mfma_f32_16x16x32_bf16 v[18:21], v[178:181], v[174:177], v[18:21]
	s_waitcnt lgkmcnt(3)
	v_mfma_f32_16x16x32_bf16 v[66:69], v[202:205], v[182:185], v[66:69]
	ds_read_b128 v[174:177], v215 offset:8192
	s_waitcnt vmcnt(13)
	s_add_u32 s8, s14, 0x1c0000
	v_mfma_f32_16x16x32_bf16 v[78:81], v[206:209], v[182:185], v[78:81]
	ds_write_b128 v190, v[220:223] offset:16384
	s_addc_u32 s9, s30, 0
	v_mfma_f32_16x16x32_bf16 v[90:93], v[210:213], v[182:185], v[90:93]
	v_mfma_f32_16x16x32_bf16 v[94:97], v[178:181], v[182:185], v[94:97]
	s_waitcnt lgkmcnt(3)
	v_mfma_f32_16x16x32_bf16 v[114:117], v[202:205], v[186:189], v[114:117]
	ds_read_b128 v[182:185], v215 offset:10240
	s_waitcnt vmcnt(12)
	s_add_u32 s8, s14, 0x1e0000
	v_mfma_f32_16x16x32_bf16 v[122:125], v[206:209], v[186:189], v[122:125]
	ds_write_b128 v190, v[216:219] offset:24576
	s_addc_u32 s9, s30, 0
	v_mfma_f32_16x16x32_bf16 v[138:141], v[210:213], v[186:189], v[138:141]
	v_mfma_f32_16x16x32_bf16 v[142:145], v[178:181], v[186:189], v[142:145]
	s_waitcnt lgkmcnt(3)
	v_mfma_f32_16x16x32_bf16 v[118:121], v[202:205], v[174:177], v[118:121]
	ds_read_b128 v[186:189], v215 offset:12288
	v_mfma_f32_16x16x32_bf16 v[126:129], v[206:209], v[174:177], v[126:129]
	v_mfma_f32_16x16x32_bf16 v[134:137], v[210:213], v[174:177], v[134:137]
	v_mfma_f32_16x16x32_bf16 v[130:133], v[178:181], v[174:177], v[130:133]
	s_waitcnt lgkmcnt(2)
	v_mfma_f32_16x16x32_bf16 v[98:101], v[202:205], v[182:185], v[98:101]
	ds_read_b128 v[174:177], v215 offset:14336
	v_mfma_f32_16x16x32_bf16 v[102:105], v[206:209], v[182:185], v[102:105]
	v_mfma_f32_16x16x32_bf16 v[110:113], v[210:213], v[182:185], v[110:113]
	v_mfma_f32_16x16x32_bf16 v[106:109], v[178:181], v[182:185], v[106:109]
	s_waitcnt lgkmcnt(1)
	v_mfma_f32_16x16x32_bf16 v[70:73], v[202:205], v[186:189], v[70:73]
	v_mfma_f32_16x16x32_bf16 v[82:85], v[206:209], v[186:189], v[82:85]
	v_mfma_f32_16x16x32_bf16 v[86:89], v[210:213], v[186:189], v[86:89]
	v_mfma_f32_16x16x32_bf16 v[74:77], v[178:181], v[186:189], v[74:77]
	s_waitcnt lgkmcnt(0)
	v_mfma_f32_16x16x32_bf16 v[42:45], v[202:205], v[174:177], v[42:45]
	v_mfma_f32_16x16x32_bf16 v[54:57], v[206:209], v[174:177], v[54:57]
	v_mfma_f32_16x16x32_bf16 v[58:61], v[210:213], v[174:177], v[58:61]
	v_mfma_f32_16x16x32_bf16 v[50:53], v[178:181], v[174:177], v[50:53]
	s_add_i32 s8, s5, 0x8000
	s_cmp_lg_u32 s5, 0x10000
	s_cselect_b32 s5, s8, 0
	s_add_i32 s8, s7, 0x8000
	s_cmp_lg_u32 s7, 0x10000
	s_waitcnt vmcnt(8)
	s_waitcnt lgkmcnt(0)
	s_barrier
	s_cselect_b32 s7, s8, 0
	s_add_u32 s0, s0, 0x80000
	s_addc_u32 s1, s1, 0
	s_add_i32 s6, s6, 0x8000
	v_add_u32_e32 v173, 0x80, v173
	s_add_i32 s0, 0, 0x18000
	v_add_u32_e32 v202, s0, v153
	v_add_u32_e32 v169, 0, v169
	v_add_u32_e32 v210, s0, v151
	v_add_u32_e32 v212, s0, v146
	ds_read_b64_tr_b16 v[172:173], v202
	ds_read_b64_tr_b16 v[174:175], v202 offset:2048
	v_add_u32_e32 v206, s0, v152
	ds_read_b128 v[176:179], v169
	ds_read_b64_tr_b16 v[180:181], v206
	ds_read_b64_tr_b16 v[182:183], v206 offset:2048
	ds_read_b128 v[184:187], v169 offset:2048
	ds_read_b64_tr_b16 v[188:189], v210
	ds_read_b64_tr_b16 v[190:191], v210 offset:2048
	ds_read_b64_tr_b16 v[192:193], v212
	ds_read_b64_tr_b16 v[194:195], v212 offset:2048
	s_waitcnt lgkmcnt(7)
	v_mfma_f32_16x16x32_bf16 v[62:65], v[172:175], v[176:179], v[62:65]
	ds_read_b128 v[196:199], v169 offset:4096
	s_waitcnt lgkmcnt(6)
	v_mfma_f32_16x16x32_bf16 v[46:49], v[180:183], v[176:179], v[46:49]
	s_waitcnt lgkmcnt(3)
	v_mfma_f32_16x16x32_bf16 v[38:41], v[188:191], v[176:179], v[38:41]
	s_waitcnt lgkmcnt(1)
	v_mfma_f32_16x16x32_bf16 v[34:37], v[192:195], v[176:179], v[34:37]
	v_mfma_f32_16x16x32_bf16 v[30:33], v[172:175], v[184:187], v[30:33]
	ds_read_b128 v[176:179], v169 offset:6144
	v_mfma_f32_16x16x32_bf16 v[26:29], v[180:183], v[184:187], v[26:29]
	v_mfma_f32_16x16x32_bf16 v[22:25], v[188:191], v[184:187], v[22:25]
	v_mfma_f32_16x16x32_bf16 v[18:21], v[192:195], v[184:187], v[18:21]
	s_waitcnt lgkmcnt(1)
	v_mfma_f32_16x16x32_bf16 v[66:69], v[172:175], v[196:199], v[66:69]
	ds_read_b128 v[184:187], v169 offset:8192
	v_mfma_f32_16x16x32_bf16 v[78:81], v[180:183], v[196:199], v[78:81]
	v_mfma_f32_16x16x32_bf16 v[90:93], v[188:191], v[196:199], v[90:93]
	v_mfma_f32_16x16x32_bf16 v[94:97], v[192:195], v[196:199], v[94:97]
	s_waitcnt lgkmcnt(1)
	v_mfma_f32_16x16x32_bf16 v[114:117], v[172:175], v[176:179], v[114:117]
	ds_read_b128 v[196:199], v169 offset:10240
	v_mfma_f32_16x16x32_bf16 v[122:125], v[180:183], v[176:179], v[122:125]
	v_mfma_f32_16x16x32_bf16 v[138:141], v[188:191], v[176:179], v[138:141]
	v_mfma_f32_16x16x32_bf16 v[142:145], v[192:195], v[176:179], v[142:145]
	ds_read_b128 v[176:179], v169 offset:12288
	ds_read_b64_tr_b16 v[200:201], v202 offset:16384
	ds_read_b64_tr_b16 v[202:203], v202 offset:18432
	s_waitcnt lgkmcnt(4)
	v_mfma_f32_16x16x32_bf16 v[118:121], v[172:175], v[184:187], v[118:121]
	v_mfma_f32_16x16x32_bf16 v[126:129], v[180:183], v[184:187], v[126:129]
	v_mfma_f32_16x16x32_bf16 v[134:137], v[188:191], v[184:187], v[134:137]
	v_mfma_f32_16x16x32_bf16 v[130:133], v[192:195], v[184:187], v[130:133]
	ds_read_b128 v[184:187], v169 offset:14336
	ds_read_b64_tr_b16 v[204:205], v206 offset:16384
	ds_read_b64_tr_b16 v[206:207], v206 offset:18432
	s_waitcnt lgkmcnt(6)
	v_mfma_f32_16x16x32_bf16 v[98:101], v[172:175], v[196:199], v[98:101]
	v_mfma_f32_16x16x32_bf16 v[102:105], v[180:183], v[196:199], v[102:105]
	v_mfma_f32_16x16x32_bf16 v[110:113], v[188:191], v[196:199], v[110:113]
	v_mfma_f32_16x16x32_bf16 v[106:109], v[192:195], v[196:199], v[106:109]
	v_add_u32_e32 v171, 0, v171
	ds_read_b128 v[196:199], v171
	ds_read_b64_tr_b16 v[208:209], v210 offset:16384
	ds_read_b64_tr_b16 v[210:211], v210 offset:18432
	s_waitcnt lgkmcnt(8)
	v_mfma_f32_16x16x32_bf16 v[70:73], v[172:175], v[176:179], v[70:73]
	v_mfma_f32_16x16x32_bf16 v[82:85], v[180:183], v[176:179], v[82:85]
	v_mfma_f32_16x16x32_bf16 v[86:89], v[188:191], v[176:179], v[86:89]
	v_mfma_f32_16x16x32_bf16 v[74:77], v[192:195], v[176:179], v[74:77]
	s_waitcnt lgkmcnt(5)
	v_mfma_f32_16x16x32_bf16 v[42:45], v[172:175], v[184:187], v[42:45]
	ds_read_b128 v[172:175], v171 offset:2048
	ds_read_b64_tr_b16 v[176:177], v212 offset:16384
	ds_read_b64_tr_b16 v[178:179], v212 offset:18432
	v_mfma_f32_16x16x32_bf16 v[54:57], v[180:183], v[184:187], v[54:57]
	v_mfma_f32_16x16x32_bf16 v[58:61], v[188:191], v[184:187], v[58:61]
	v_mfma_f32_16x16x32_bf16 v[50:53], v[192:195], v[184:187], v[50:53]
	ds_read_b128 v[180:183], v171 offset:4096
	s_waitcnt vmcnt(3)
	v_add_u32_e32 v168, s38, v168
	s_waitcnt lgkmcnt(6)
	v_mfma_f32_16x16x32_bf16 v[62:65], v[200:203], v[196:199], v[62:65]
	ds_write_b128 v168, v[14:17]
	v_mfma_f32_16x16x32_bf16 v[46:49], v[204:207], v[196:199], v[46:49]
	s_waitcnt lgkmcnt(5)
	v_mfma_f32_16x16x32_bf16 v[38:41], v[208:211], v[196:199], v[38:41]
	s_waitcnt lgkmcnt(2)
	v_mfma_f32_16x16x32_bf16 v[14:17], v[176:179], v[196:199], v[34:37]
	s_nop 2
	ds_read_b128 v[34:37], v171 offset:6144
	s_waitcnt vmcnt(2)
	v_mfma_f32_16x16x32_bf16 v[30:33], v[200:203], v[172:175], v[30:33]
	ds_write_b128 v168, v[10:13] offset:8192
	v_mfma_f32_16x16x32_bf16 v[26:29], v[204:207], v[172:175], v[26:29]
	v_mfma_f32_16x16x32_bf16 v[22:25], v[208:211], v[172:175], v[22:25]
	v_mfma_f32_16x16x32_bf16 v[10:13], v[176:179], v[172:175], v[18:21]
	s_waitcnt lgkmcnt(3)
	v_mfma_f32_16x16x32_bf16 v[18:21], v[200:203], v[180:183], v[66:69]
	v_mfma_f32_16x16x32_bf16 v[66:69], v[204:207], v[180:183], v[78:81]
	v_mfma_f32_16x16x32_bf16 v[78:81], v[208:211], v[180:183], v[90:93]
	s_nop 2
	ds_read_b128 v[90:93], v171 offset:8192
	s_waitcnt vmcnt(1)
	ds_write_b128 v168, v[6:9] offset:16384
	v_mfma_f32_16x16x32_bf16 v[6:9], v[176:179], v[180:183], v[94:97]
	s_waitcnt lgkmcnt(3)
	v_mfma_f32_16x16x32_bf16 v[94:97], v[200:203], v[34:37], v[114:117]
	v_mfma_f32_16x16x32_bf16 v[114:117], v[204:207], v[34:37], v[122:125]
	v_mfma_f32_16x16x32_bf16 v[122:125], v[208:211], v[34:37], v[138:141]
	s_nop 2
	ds_read_b128 v[138:141], v171 offset:10240
	s_waitcnt vmcnt(0)
	ds_write_b128 v168, v[2:5] offset:24576
	v_mfma_f32_16x16x32_bf16 v[2:5], v[176:179], v[34:37], v[142:145]
	s_waitcnt lgkmcnt(3)
	v_mfma_f32_16x16x32_bf16 v[34:37], v[200:203], v[90:93], v[118:121]
	v_mfma_f32_16x16x32_bf16 v[118:121], v[204:207], v[90:93], v[126:129]
	v_mfma_f32_16x16x32_bf16 v[126:129], v[208:211], v[90:93], v[134:137]
	s_nop 2
	ds_read_b128 v[134:137], v171 offset:12288
	v_mfma_f32_16x16x32_bf16 v[90:93], v[176:179], v[90:93], v[130:133]
	s_waitcnt lgkmcnt(2)
	v_mfma_f32_16x16x32_bf16 v[98:101], v[200:203], v[138:141], v[98:101]
	s_nop 0
	ds_read_b128 v[130:133], v171 offset:14336
	v_mfma_f32_16x16x32_bf16 v[102:105], v[204:207], v[138:141], v[102:105]
	v_mfma_f32_16x16x32_bf16 v[110:113], v[208:211], v[138:141], v[110:113]
	v_mfma_f32_16x16x32_bf16 v[106:109], v[176:179], v[138:141], v[106:109]
	s_waitcnt lgkmcnt(1)
	v_mfma_f32_16x16x32_bf16 v[70:73], v[200:203], v[134:137], v[70:73]
	v_mfma_f32_16x16x32_bf16 v[82:85], v[204:207], v[134:137], v[82:85]
	v_mfma_f32_16x16x32_bf16 v[86:89], v[208:211], v[134:137], v[86:89]
	v_mfma_f32_16x16x32_bf16 v[74:77], v[176:179], v[134:137], v[74:77]
	s_waitcnt lgkmcnt(0)
	v_mfma_f32_16x16x32_bf16 v[42:45], v[200:203], v[130:133], v[42:45]
	v_mfma_f32_16x16x32_bf16 v[54:57], v[204:207], v[130:133], v[54:57]
	v_mfma_f32_16x16x32_bf16 v[58:61], v[208:211], v[130:133], v[58:61]
	v_mfma_f32_16x16x32_bf16 v[50:53], v[176:179], v[130:133], v[50:53]
	s_waitcnt lgkmcnt(0)
	s_barrier
	v_add_u32_e32 v153, s38, v153
	v_add_u32_e32 v152, s38, v152
	v_add_u32_e32 v151, s38, v151
	ds_read_b64_tr_b16 v[130:131], v153
	ds_read_b64_tr_b16 v[132:133], v153 offset:2048
	ds_read_b64_tr_b16 v[134:135], v152
	ds_read_b64_tr_b16 v[136:137], v152 offset:2048
	ds_read_b128 v[138:141], v169 offset:32768
	ds_read_b64_tr_b16 v[142:143], v151
	ds_read_b128 v[172:175], v169 offset:34816
	ds_read_b128 v[176:179], v169 offset:36864
	ds_read_b64_tr_b16 v[144:145], v151 offset:2048
	v_add_u32_e32 v146, s38, v146
	ds_read_b64_tr_b16 v[180:181], v146
	ds_read_b64_tr_b16 v[182:183], v146 offset:2048
	s_waitcnt lgkmcnt(6)
	v_mfma_f32_16x16x32_bf16 v[62:65], v[130:133], v[138:141], v[62:65]
	v_mfma_f32_16x16x32_bf16 v[46:49], v[134:137], v[138:141], v[46:49]
	s_waitcnt lgkmcnt(2)
	v_mfma_f32_16x16x32_bf16 v[38:41], v[142:145], v[138:141], v[38:41]
	s_waitcnt lgkmcnt(0)
	v_mfma_f32_16x16x32_bf16 v[14:17], v[180:183], v[138:141], v[14:17]
	v_mfma_f32_16x16x32_bf16 v[30:33], v[130:133], v[172:175], v[30:33]
	ds_read_b128 v[138:141], v169 offset:38912
	v_mfma_f32_16x16x32_bf16 v[26:29], v[134:137], v[172:175], v[26:29]
	v_mfma_f32_16x16x32_bf16 v[22:25], v[142:145], v[172:175], v[22:25]
	v_mfma_f32_16x16x32_bf16 v[10:13], v[180:183], v[172:175], v[10:13]
	v_mfma_f32_16x16x32_bf16 v[18:21], v[130:133], v[176:179], v[18:21]
	ds_read_b128 v[172:175], v169 offset:40960
	v_mfma_f32_16x16x32_bf16 v[66:69], v[134:137], v[176:179], v[66:69]
	v_mfma_f32_16x16x32_bf16 v[78:81], v[142:145], v[176:179], v[78:81]
	v_mfma_f32_16x16x32_bf16 v[6:9], v[180:183], v[176:179], v[6:9]
	s_waitcnt lgkmcnt(1)
	v_mfma_f32_16x16x32_bf16 v[176:179], v[130:133], v[138:141], v[94:97]
	s_nop 2
	ds_read_b128 v[94:97], v169 offset:43008
	v_mfma_f32_16x16x32_bf16 v[2:5], v[180:183], v[138:141], v[2:5]
	v_mfma_f32_16x16x32_bf16 v[184:187], v[134:137], v[138:141], v[114:117]
	v_mfma_f32_16x16x32_bf16 v[188:191], v[142:145], v[138:141], v[122:125]
	s_nop 1
	ds_read_b128 v[114:117], v169 offset:45056
	ds_read_b64_tr_b16 v[196:197], v153 offset:16384
	ds_read_b64_tr_b16 v[198:199], v153 offset:18432
	s_waitcnt lgkmcnt(4)
	v_mfma_f32_16x16x32_bf16 v[34:37], v[130:133], v[172:175], v[34:37]
	v_mfma_f32_16x16x32_bf16 v[138:141], v[134:137], v[172:175], v[118:121]
	v_mfma_f32_16x16x32_bf16 v[192:195], v[142:145], v[172:175], v[126:129]
	v_mfma_f32_16x16x32_bf16 v[172:175], v[180:183], v[172:175], v[90:93]
	s_nop 2
	ds_read_b128 v[90:93], v169 offset:47104
	ds_read_b64_tr_b16 v[212:213], v152 offset:16384
	ds_read_b64_tr_b16 v[214:215], v152 offset:18432
	s_waitcnt lgkmcnt(6)
	v_mfma_f32_16x16x32_bf16 v[200:203], v[130:133], v[94:97], v[98:101]
	v_mfma_f32_16x16x32_bf16 v[204:207], v[134:137], v[94:97], v[102:105]
	v_mfma_f32_16x16x32_bf16 v[208:211], v[142:145], v[94:97], v[110:113]
	v_mfma_f32_16x16x32_bf16 v[216:219], v[180:183], v[94:97], v[106:109]
	s_waitcnt lgkmcnt(5)
	v_mfma_f32_16x16x32_bf16 v[220:223], v[130:133], v[114:117], v[70:73]
	s_nop 2
	ds_read_b128 v[70:73], v171 offset:32768
	ds_read_b64_tr_b16 v[232:233], v151 offset:16384
	ds_read_b64_tr_b16 v[234:235], v151 offset:18432
	v_mfma_f32_16x16x32_bf16 v[224:227], v[134:137], v[114:117], v[82:85]
	v_mfma_f32_16x16x32_bf16 v[228:231], v[142:145], v[114:117], v[86:89]
	v_mfma_f32_16x16x32_bf16 v[236:239], v[180:183], v[114:117], v[74:77]
	s_waitcnt lgkmcnt(5)
	v_mfma_f32_16x16x32_bf16 v[130:133], v[130:133], v[90:93], v[42:45]
	s_nop 2
	ds_read_b128 v[42:45], v171 offset:34816
	ds_read_b64_tr_b16 v[240:241], v146 offset:16384
	ds_read_b64_tr_b16 v[242:243], v146 offset:18432
	v_mfma_f32_16x16x32_bf16 v[134:137], v[134:137], v[90:93], v[54:57]
	v_mfma_f32_16x16x32_bf16 v[142:145], v[142:145], v[90:93], v[58:61]
	v_mfma_f32_16x16x32_bf16 v[180:183], v[180:183], v[90:93], v[50:53]
	s_waitcnt lgkmcnt(3)
	v_mfma_f32_16x16x32_bf16 v[118:121], v[232:235], v[70:73], v[38:41]
	s_nop 2
	ds_read_b128 v[38:41], v171 offset:36864
	v_mfma_f32_16x16x32_bf16 v[126:129], v[196:199], v[70:73], v[62:65]
	v_mfma_f32_16x16x32_bf16 v[122:125], v[212:215], v[70:73], v[46:49]
	s_waitcnt lgkmcnt(1)
	v_mfma_f32_16x16x32_bf16 v[114:117], v[240:243], v[70:73], v[14:17]
	s_nop 2
	ds_read_b128 v[14:17], v171 offset:38912
	v_mfma_f32_16x16x32_bf16 v[110:113], v[196:199], v[42:45], v[30:33]
	v_mfma_f32_16x16x32_bf16 v[106:109], v[212:215], v[42:45], v[26:29]
	v_mfma_f32_16x16x32_bf16 v[102:105], v[232:235], v[42:45], v[22:25]
	v_mfma_f32_16x16x32_bf16 v[98:101], v[240:243], v[42:45], v[10:13]
	s_nop 2
	ds_read_b128 v[10:13], v171 offset:40960
	s_waitcnt lgkmcnt(2)
	v_mfma_f32_16x16x32_bf16 v[94:97], v[196:199], v[38:41], v[18:21]
	v_mfma_f32_16x16x32_bf16 v[90:93], v[212:215], v[38:41], v[66:69]
	v_mfma_f32_16x16x32_bf16 v[86:89], v[232:235], v[38:41], v[78:81]
	v_mfma_f32_16x16x32_bf16 v[82:85], v[240:243], v[38:41], v[6:9]
	s_nop 2
	ds_read_b128 v[6:9], v171 offset:43008
	s_waitcnt lgkmcnt(2)
	v_mfma_f32_16x16x32_bf16 v[78:81], v[196:199], v[14:17], v[176:179]
	v_mfma_f32_16x16x32_bf16 v[74:77], v[212:215], v[14:17], v[184:187]
	v_mfma_f32_16x16x32_bf16 v[70:73], v[232:235], v[14:17], v[188:191]
	v_mfma_f32_16x16x32_bf16 v[66:69], v[240:243], v[14:17], v[2:5]
	s_nop 2
	ds_read_b128 v[2:5], v171 offset:45056
	s_waitcnt lgkmcnt(2)
	v_mfma_f32_16x16x32_bf16 v[62:65], v[196:199], v[10:13], v[34:37]
	v_mfma_f32_16x16x32_bf16 v[58:61], v[212:215], v[10:13], v[138:141]
	v_mfma_f32_16x16x32_bf16 v[54:57], v[232:235], v[10:13], v[192:195]
	v_mfma_f32_16x16x32_bf16 v[50:53], v[240:243], v[10:13], v[172:175]
	s_waitcnt lgkmcnt(1)
	v_mfma_f32_16x16x32_bf16 v[46:49], v[196:199], v[6:9], v[200:203]
	ds_read_b128 v[138:141], v171 offset:47104
	v_mfma_f32_16x16x32_bf16 v[42:45], v[212:215], v[6:9], v[204:207]
	v_mfma_f32_16x16x32_bf16 v[38:41], v[232:235], v[6:9], v[208:211]
	v_mfma_f32_16x16x32_bf16 v[34:37], v[240:243], v[6:9], v[216:219]
	s_waitcnt lgkmcnt(1)
	v_mfma_f32_16x16x32_bf16 v[30:33], v[196:199], v[2:5], v[220:223]
	v_mfma_f32_16x16x32_bf16 v[26:29], v[212:215], v[2:5], v[224:227]
	v_mfma_f32_16x16x32_bf16 v[22:25], v[232:235], v[2:5], v[228:231]
	v_mfma_f32_16x16x32_bf16 v[18:21], v[240:243], v[2:5], v[236:239]
	s_waitcnt lgkmcnt(0)
	v_mfma_f32_16x16x32_bf16 v[14:17], v[196:199], v[138:141], v[130:133]
	v_mfma_f32_16x16x32_bf16 v[10:13], v[212:215], v[138:141], v[134:137]
	v_mfma_f32_16x16x32_bf16 v[6:9], v[232:235], v[138:141], v[142:145]
	v_mfma_f32_16x16x32_bf16 v[2:5], v[240:243], v[138:141], v[180:183]
	s_waitcnt lgkmcnt(0)
	s_barrier
	v_mov_b32_e32 v151, v155
	v_mov_b32_e32 v168, v1
	s_cmpk_gt_i32 s28, 0x3ff
	s_mov_b64 s[0:1], -1
	s_cbranch_scc1 .LBB0_607
	s_add_i32 s0, s52, s50
	v_add_u32_e32 v140, s0, v168
	s_lshl_b32 s0, s51, 6
	s_or_b32 s0, s0, s28
	v_lshlrev_b32_e32 v132, 2, v151
	v_add_u32_e32 v146, s0, v132
	v_ashrrev_i32_e32 v141, 31, v140
	v_lshlrev_b64 v[142:143], 11, v[140:141]
	v_cmp_lt_i32_e64 s[4:5], s39, v146
	s_and_saveexec_b64 s[0:1], s[4:5]
	s_xor_b64 s[0:1], exec, s[0:1]
	s_cbranch_execz .LBB0_442
	v_cmp_lt_u32_e32 vcc, s41, v146
	s_and_saveexec_b64 s[2:3], vcc
	s_xor_b64 s[2:3], exec, s[2:3]
	s_cbranch_execz .LBB0_439
	v_cmp_lt_u32_e32 vcc, s42, v146
	v_cvt_pk_bf16_f32 v130, v126, v127
	v_cvt_pk_bf16_f32 v131, v128, v129
	s_and_saveexec_b64 s[6:7], vcc
	s_xor_b64 s[6:7], exec, s[6:7]
	s_cbranch_execz .LBB0_436
	v_lshl_add_u64 v[134:135], s[24:25], 0, v[142:143]
	v_lshl_add_u64 v[134:135], v[146:147], 1, v[134:135]
	v_add_co_u32_e32 v134, vcc, 0xfffff000, v134
	s_nop 1
	v_addc_co_u32_e32 v135, vcc, -1, v135, vcc
	global_store_dwordx2 v[134:135], v[130:131], off offset:-2048
